# gdn_scan: one dword load per step touches the u0 tile two chunks ahead (L2 warm-up), u0 wait vmcnt(33), on top of v90
# baseline (speedup 1.0000x reference)
.LBB0_490:
	s_bitcmp1_b32 s35, 0
	s_cselect_b32 s26, 0xea00, 0
	v_add_u32_e32 v159, s26, v157
	v_add_u32_e32 v190, v159, v155
	ds_read2_b64 v[68:71], v190 offset1:2
	ds_read2_b64 v[84:87], v190 offset0:4 offset1:6
	ds_read2_b64 v[88:91], v190 offset0:8 offset1:10
	ds_read2_b64 v[92:95], v190 offset0:12 offset1:14
	ds_read2_b64 v[96:99], v190 offset0:16 offset1:18
	ds_read2_b64 v[100:103], v190 offset0:20 offset1:22
	ds_read2_b64 v[104:107], v190 offset0:24 offset1:26
	ds_read2_b64 v[108:111], v190 offset0:28 offset1:30
	v_add_u32_e32 v112, 0x2000, v190
	v_add_u32_e32 v182, 0x2000, v190
	v_add_u32_e32 v186, 0x2000, v190
	v_add_u32_e32 v214, 0x2000, v190
	ds_read2_b64 v[112:115], v112 offset0:48 offset1:50
	ds_read2_b64 v[182:185], v182 offset0:52 offset1:54
	ds_read2_b64 v[186:189], v186 offset0:56 offset1:58
	ds_read2_b64 v[214:217], v214 offset0:60 offset1:62
	v_cvt_pk_bf16_f32 v116, v52, v53
	v_cvt_pk_bf16_f32 v117, v54, v55
	v_cvt_pk_bf16_f32 v118, v56, v57
	v_cvt_pk_bf16_f32 v119, v58, v59
	v_cvt_pk_bf16_f32 v120, v60, v61
	v_cvt_pk_bf16_f32 v121, v62, v63
	v_cvt_pk_bf16_f32 v122, v64, v65
	v_cvt_pk_bf16_f32 v123, v66, v67
	v_cvt_pk_bf16_f32 v124, v36, v37
	v_cvt_pk_bf16_f32 v125, v38, v39
	v_cvt_pk_bf16_f32 v126, v40, v41
	v_cvt_pk_bf16_f32 v127, v42, v43
	v_cvt_pk_bf16_f32 v128, v44, v45
	v_cvt_pk_bf16_f32 v129, v46, v47
	v_cvt_pk_bf16_f32 v130, v48, v49
	v_cvt_pk_bf16_f32 v131, v50, v51
	v_cvt_pk_bf16_f32 v132, v20, v21
	v_cvt_pk_bf16_f32 v133, v22, v23
	v_cvt_pk_bf16_f32 v134, v24, v25
	v_cvt_pk_bf16_f32 v135, v26, v27
	v_cvt_pk_bf16_f32 v136, v28, v29
	v_cvt_pk_bf16_f32 v137, v30, v31
	v_cvt_pk_bf16_f32 v138, v32, v33
	v_cvt_pk_bf16_f32 v139, v34, v35
	v_cvt_pk_bf16_f32 v140, v4, v5
	v_cvt_pk_bf16_f32 v141, v6, v7
	v_cvt_pk_bf16_f32 v142, v8, v9
	v_cvt_pk_bf16_f32 v143, v10, v11
	v_cvt_pk_bf16_f32 v144, v12, v13
	v_cvt_pk_bf16_f32 v145, v14, v15
	v_cvt_pk_bf16_f32 v146, v16, v17
	v_cvt_pk_bf16_f32 v147, v18, v19
	s_waitcnt lgkmcnt(4)
	v_mfma_f32_32x32x16_bf16 v[68:83], v[68:71], v[116:119], 0
	v_mfma_f32_32x32x16_bf16 v[68:83], v[84:87], v[120:123], v[68:83]
	v_add_u32_e32 v84, 0x2000, v190
	ds_read2_b64 v[84:87], v84 offset0:32 offset1:34
	v_mfma_f32_32x32x16_bf16 v[68:83], v[88:91], v[124:127], v[68:83]
	v_mfma_f32_32x32x16_bf16 v[68:83], v[92:95], v[128:131], v[68:83]
	v_mfma_f32_32x32x16_bf16 v[68:83], v[96:99], v[132:135], v[68:83]
	v_mfma_f32_32x32x16_bf16 v[68:83], v[100:103], v[136:139], v[68:83]
	v_add_u32_e32 v100, 0x2000, v190
	ds_read2_b64 v[100:103], v100 offset0:36 offset1:38
	v_mfma_f32_32x32x16_bf16 v[68:83], v[104:107], v[140:143], v[68:83]
	v_add_u32_e32 v104, 0x2000, v190
	ds_read2_b64 v[104:107], v104 offset0:40 offset1:42
	v_mfma_f32_32x32x16_bf16 v[68:83], v[108:111], v[144:147], v[68:83]
	v_add_u32_e32 v108, 0x2000, v190
	ds_read2_b64 v[108:111], v108 offset0:44 offset1:46
	v_add_u32_e32 v88, 0x2000, v190
	s_waitcnt lgkmcnt(3)
	v_mfma_f32_32x32x16_bf16 v[84:99], v[84:87], v[116:119], 0
	s_waitcnt lgkmcnt(2)
	v_mfma_f32_32x32x16_bf16 v[84:99], v[100:103], v[120:123], v[84:99]
	s_waitcnt lgkmcnt(1)
	v_mfma_f32_32x32x16_bf16 v[84:99], v[104:107], v[124:127], v[84:99]
	s_waitcnt lgkmcnt(0)
	v_mfma_f32_32x32x16_bf16 v[84:99], v[108:111], v[128:131], v[84:99]
	v_mfma_f32_32x32x16_bf16 v[84:99], v[112:115], v[132:135], v[84:99]
	v_mfma_f32_32x32x16_bf16 v[84:99], v[182:185], v[136:139], v[84:99]
	v_mfma_f32_32x32x16_bf16 v[84:99], v[186:189], v[140:143], v[84:99]
	v_mfma_f32_32x32x16_bf16 v[84:99], v[214:217], v[144:147], v[84:99]
	s_waitcnt vmcnt(33)
	v_mov_b32_e32 v200, v201
	v_sub_f32_e32 v81, v197, v81
	v_sub_f32_e32 v80, v196, v80
	v_sub_f32_e32 v71, v165, v71
	v_sub_f32_e32 v70, v164, v70
	v_sub_f32_e32 v69, v167, v69
	v_sub_f32_e32 v68, v166, v68
	v_cvt_pk_bf16_f32 v106, v80, v81
	s_nop 3
	v_sub_f32_e32 v80, v175, v87
	v_sub_f32_e32 v81, v174, v86
	v_sub_f32_e32 v83, v199, v83
	v_sub_f32_e32 v82, v198, v82
	v_sub_f32_e32 v79, v195, v79
	v_sub_f32_e32 v78, v194, v78
	v_sub_f32_e32 v77, v181, v77
	v_sub_f32_e32 v76, v180, v76
	v_sub_f32_e32 v75, v171, v75
	v_sub_f32_e32 v74, v170, v74
	v_sub_f32_e32 v73, v169, v73
	v_sub_f32_e32 v72, v168, v72
	v_cvt_pk_bf16_f32 v100, v68, v69
	v_cvt_pk_bf16_f32 v101, v70, v71
	v_sub_f32_e32 v68, v179, v91
	v_sub_f32_e32 v69, v178, v90
	v_sub_f32_e32 v70, v177, v89
	v_sub_f32_e32 v71, v176, v88
	v_cvt_pk_bf16_f32 v109, v81, v80
	v_add_u32_e32 v80, 0x4000, v190
	v_cvt_pk_bf16_f32 v102, v72, v73
	v_cvt_pk_bf16_f32 v103, v74, v75
	v_cvt_pk_bf16_f32 v104, v76, v77
	v_cvt_pk_bf16_f32 v105, v78, v79
	v_cvt_pk_bf16_f32 v107, v82, v83
	v_sub_f32_e32 v72, v209, v99
	v_sub_f32_e32 v73, v208, v98
	v_sub_f32_e32 v74, v207, v97
	v_sub_f32_e32 v75, v206, v96
	v_sub_f32_e32 v76, v205, v95
	v_sub_f32_e32 v77, v204, v94
	v_sub_f32_e32 v78, v203, v93
	v_sub_f32_e32 v79, v202, v92
	v_sub_f32_e32 v82, v173, v85
	v_sub_f32_e32 v83, v172, v84
	v_cvt_pk_bf16_f32 v110, v71, v70
	v_cvt_pk_bf16_f32 v111, v69, v68
	ds_read2_b64 v[68:71], v80 offset0:64 offset1:66
	ds_read2_b64 v[84:87], v80 offset0:68 offset1:70
	ds_read2_b64 v[88:91], v80 offset0:72 offset1:74
	ds_read2_b64 v[92:95], v80 offset0:76 offset1:78
	ds_read2_b64 v[96:99], v80 offset0:80 offset1:82
	ds_read2_b64 v[164:167], v80 offset0:84 offset1:86
	ds_read2_b64 v[168:171], v80 offset0:88 offset1:90
	ds_read2_b64 v[172:175], v80 offset0:92 offset1:94
	v_add_u32_e32 v176, 0x6000, v190
	v_add_u32_e32 v180, 0x6000, v190
	v_add_u32_e32 v184, 0x6000, v190
	v_add_u32_e32 v194, 0x6000, v190
	ds_read2_b64 v[176:179], v176 offset0:112 offset1:114
	ds_read2_b64 v[180:183], v180 offset0:116 offset1:118
	ds_read2_b64 v[184:187], v184 offset0:120 offset1:122
	ds_read2_b64 v[194:197], v194 offset0:124 offset1:126
	v_cvt_pk_bf16_f32 v108, v83, v82
	v_cvt_pk_bf16_f32 v112, v79, v78
	v_cvt_pk_bf16_f32 v113, v77, v76
	v_cvt_pk_bf16_f32 v114, v75, v74
	v_cvt_pk_bf16_f32 v115, v73, v72
	s_waitcnt lgkmcnt(11)
	v_mfma_f32_32x32x16_bf16 v[68:83], v[68:71], v[116:119], 0
	s_waitcnt lgkmcnt(10)
	v_mfma_f32_32x32x16_bf16 v[68:83], v[84:87], v[120:123], v[68:83]
	v_add_u32_e32 v84, 0x6000, v190
	ds_read2_b64 v[84:87], v84 offset0:96 offset1:98
	s_waitcnt lgkmcnt(10)
	v_mfma_f32_32x32x16_bf16 v[68:83], v[88:91], v[124:127], v[68:83]
	s_waitcnt lgkmcnt(9)
	v_mfma_f32_32x32x16_bf16 v[68:83], v[92:95], v[128:131], v[68:83]
	s_waitcnt lgkmcnt(8)
	v_mfma_f32_32x32x16_bf16 v[68:83], v[96:99], v[132:135], v[68:83]
	s_waitcnt lgkmcnt(7)
	v_mfma_f32_32x32x16_bf16 v[68:83], v[164:167], v[136:139], v[68:83]
	v_add_u32_e32 v164, 0x6000, v190
	ds_read2_b64 v[164:167], v164 offset0:100 offset1:102
	s_waitcnt lgkmcnt(7)
	v_mfma_f32_32x32x16_bf16 v[68:83], v[168:171], v[140:143], v[68:83]
	v_add_u32_e32 v168, 0x6000, v190
	ds_read2_b64 v[168:171], v168 offset0:104 offset1:106
	s_waitcnt lgkmcnt(7)
	v_mfma_f32_32x32x16_bf16 v[68:83], v[172:175], v[144:147], v[68:83]
	v_add_u32_e32 v172, 0x6000, v190
	ds_read2_b64 v[172:175], v172 offset0:108 offset1:110
	v_add_u32_e32 v88, 0x6000, v190
	s_waitcnt lgkmcnt(3)
	v_mfma_f32_32x32x16_bf16 v[84:99], v[84:87], v[116:119], 0
	v_add_u32_e32 v116, v159, v153
	v_add_u32_e32 v116, 0x8000, v116
	ds_read2_b64 v[116:119], v116 offset0:128 offset1:130
	s_waitcnt lgkmcnt(3)
	v_mfma_f32_32x32x16_bf16 v[84:99], v[164:167], v[120:123], v[84:99]
	v_add_u32_e32 v120, v159, v153
	v_add_u32_e32 v120, 0x8000, v120
	ds_read2_b64 v[120:123], v120 offset0:132 offset1:134
	s_waitcnt lgkmcnt(3)
	v_mfma_f32_32x32x16_bf16 v[84:99], v[168:171], v[124:127], v[84:99]
	v_add_u32_e32 v124, v159, v153
	v_add_u32_e32 v124, 0x8000, v124
	ds_read2_b64 v[124:127], v124 offset0:136 offset1:138
	s_waitcnt lgkmcnt(3)
	v_mfma_f32_32x32x16_bf16 v[84:99], v[172:175], v[128:131], v[84:99]
	v_add_u32_e32 v128, v159, v153
	v_add_u32_e32 v128, 0x8000, v128
	ds_read2_b64 v[128:131], v128 offset0:140 offset1:142
	v_mfma_f32_32x32x16_bf16 v[84:99], v[176:179], v[132:135], v[84:99]
	v_add_u32_e32 v132, v159, v153
	v_add_u32_e32 v132, 0x9000, v132
	ds_read2_b64 v[132:135], v132 offset0:160 offset1:162
	v_mfma_f32_32x32x16_bf16 v[84:99], v[180:183], v[136:139], v[84:99]
	v_add_u32_e32 v136, v159, v153
	v_add_u32_e32 v136, 0x9000, v136
	ds_read2_b64 v[136:139], v136 offset0:164 offset1:166
	v_mfma_f32_32x32x16_bf16 v[84:99], v[184:187], v[140:143], v[84:99]
	v_add_u32_e32 v140, v159, v153
	v_add_u32_e32 v140, 0x9000, v140
	ds_read2_b64 v[140:143], v140 offset0:168 offset1:170
	v_mfma_f32_32x32x16_bf16 v[84:99], v[194:197], v[144:147], v[84:99]
	v_add_u32_e32 v144, v159, v153
	v_add_u32_e32 v144, 0x9000, v144
	ds_read2_b64 v[144:147], v144 offset0:172 offset1:174
	v_add_u32_e32 v159, v159, v153
	v_lshl_add_u64 v[182:183], s[6:7], 0, v[162:163]
	s_mov_b32 s26, 0x41a20000
	v_add_co_u32_e32 v218, vcc, s26, v182
	s_nop 1
	v_addc_co_u32_e32 v219, vcc, 0, v183, vcc
	s_mov_b32 s26, 0x41a21000
	v_add_co_u32_e32 v220, vcc, s26, v182
	s_nop 1
	v_addc_co_u32_e32 v221, vcc, 0, v183, vcc
	s_mov_b32 s26, 0x41a24000
	v_add_co_u32_e32 v222, vcc, s26, v182
	s_nop 1
	v_addc_co_u32_e32 v223, vcc, 0, v183, vcc
	s_mov_b32 s26, 0x41a25000
	v_add_co_u32_e32 v224, vcc, s26, v182
	s_nop 1
	v_addc_co_u32_e32 v225, vcc, 0, v183, vcc
	global_load_dword v166, v[218:219], off
	global_load_dword v167, v[218:219], off offset:2048
	global_load_dword v164, v[220:221], off
	global_load_dword v165, v[220:221], off offset:2048
	global_load_dword v168, v[222:223], off
	global_load_dword v169, v[222:223], off offset:2048
	global_load_dword v170, v[224:225], off
	global_load_dword v171, v[224:225], off offset:2048
	s_mov_b32 s26, 0x41a28000
	v_add_co_u32_e32 v218, vcc, s26, v182
	s_nop 1
	v_addc_co_u32_e32 v219, vcc, 0, v183, vcc
	s_mov_b32 s26, 0x41a29000
	v_add_co_u32_e32 v220, vcc, s26, v182
	s_nop 1
	v_addc_co_u32_e32 v221, vcc, 0, v183, vcc
	s_mov_b32 s26, 0x41a2c000
	v_add_co_u32_e32 v222, vcc, s26, v182
	s_nop 1
	v_addc_co_u32_e32 v223, vcc, 0, v183, vcc
	s_mov_b32 s26, 0x41a2d000
	v_add_co_u32_e32 v224, vcc, s26, v182
	s_nop 1
	v_addc_co_u32_e32 v225, vcc, 0, v183, vcc
	global_load_dword v180, v[218:219], off
	global_load_dword v181, v[218:219], off offset:2048
	global_load_dword v194, v[220:221], off
	global_load_dword v195, v[220:221], off offset:2048
	global_load_dword v196, v[222:223], off
	global_load_dword v197, v[222:223], off offset:2048
	global_load_dword v198, v[224:225], off
	global_load_dword v199, v[224:225], off offset:2048
	s_mov_b32 s26, 0x41a30000
	v_add_co_u32_e32 v218, vcc, s26, v182
	s_nop 1
	v_addc_co_u32_e32 v219, vcc, 0, v183, vcc
	s_mov_b32 s26, 0x41a31000
	v_add_co_u32_e32 v220, vcc, s26, v182
	s_nop 1
	v_addc_co_u32_e32 v221, vcc, 0, v183, vcc
	s_mov_b32 s26, 0x41a34000
	v_add_co_u32_e32 v222, vcc, s26, v182
	s_nop 1
	v_addc_co_u32_e32 v223, vcc, 0, v183, vcc
	s_mov_b32 s26, 0x41a35000
	v_add_co_u32_e32 v224, vcc, s26, v182
	s_nop 1
	v_addc_co_u32_e32 v225, vcc, 0, v183, vcc
	global_load_dword v172, v[218:219], off
	global_load_dword v173, v[218:219], off offset:2048
	global_load_dword v174, v[220:221], off
	global_load_dword v175, v[220:221], off offset:2048
	global_load_dword v176, v[222:223], off
	global_load_dword v177, v[222:223], off offset:2048
	global_load_dword v178, v[224:225], off
	global_load_dword v179, v[224:225], off offset:2048
	s_mov_b32 s26, 0x41a38000
	v_add_co_u32_e32 v218, vcc, s26, v182
	s_nop 1
	v_addc_co_u32_e32 v219, vcc, 0, v183, vcc
	s_mov_b32 s26, 0x41a39000
	v_add_co_u32_e32 v220, vcc, s26, v182
	s_nop 1
	v_addc_co_u32_e32 v221, vcc, 0, v183, vcc
	s_mov_b32 s26, 0x41a3c000
	v_add_co_u32_e32 v222, vcc, s26, v182
	s_nop 1
	v_addc_co_u32_e32 v223, vcc, 0, v183, vcc
	s_mov_b32 s26, 0x41a3d000
	v_add_co_u32_e32 v224, vcc, s26, v182
	s_nop 1
	v_addc_co_u32_e32 v225, vcc, 0, v183, vcc
	global_load_dword v202, v[218:219], off
	global_load_dword v203, v[218:219], off offset:2048
	global_load_dword v204, v[220:221], off
	global_load_dword v205, v[220:221], off offset:2048
	global_load_dword v206, v[222:223], off
	global_load_dword v207, v[222:223], off offset:2048
	global_load_dword v208, v[224:225], off
	global_load_dword v209, v[224:225], off offset:2048
	s_add_i32 s35, s35, 1
	s_add_u32 s26, s6, s28
	s_addc_u32 s27, s7, s29
	v_mov_b64_e32 v[232:233], s[26:27]
	global_load_dword v201, v[232:233], off
	s_waitcnt lgkmcnt(7)
	v_mfma_f32_32x32x16_bf16 v[68:83], v[116:119], v[100:103], v[68:83]
	s_waitcnt lgkmcnt(3)
	v_mfma_f32_32x32x16_bf16 v[84:99], v[132:135], v[100:103], v[84:99]
	v_mfma_f32_32x32x16_bf16 v[68:83], v[120:123], v[104:107], v[68:83]
	s_waitcnt lgkmcnt(2)
	v_mfma_f32_32x32x16_bf16 v[84:99], v[136:139], v[104:107], v[84:99]
	v_mfma_f32_32x32x16_bf16 v[68:83], v[124:127], v[108:111], v[68:83]
	s_waitcnt lgkmcnt(1)
	v_mfma_f32_32x32x16_bf16 v[84:99], v[140:143], v[108:111], v[84:99]
	v_mfma_f32_32x32x16_bf16 v[68:83], v[128:131], v[112:115], v[68:83]
	s_waitcnt lgkmcnt(0)
	v_mfma_f32_32x32x16_bf16 v[84:99], v[144:147], v[112:115], v[84:99]
	v_add_u32_e32 v116, 0xa000, v159
	ds_read2_b64 v[116:119], v116 offset0:192 offset1:194
	v_add_u32_e32 v120, 0xa000, v159
	ds_read2_b64 v[120:123], v120 offset0:196 offset1:198
	v_add_u32_e32 v124, 0xa000, v159
	ds_read2_b64 v[124:127], v124 offset0:200 offset1:202
	v_add_u32_e32 v128, 0xa000, v159
	ds_read2_b64 v[128:131], v128 offset0:204 offset1:206
	v_add_u32_e32 v132, 0xb000, v159
	ds_read2_b64 v[132:135], v132 offset0:224 offset1:226
	v_add_u32_e32 v136, 0xb000, v159
	ds_read2_b64 v[136:139], v136 offset0:228 offset1:230
	v_add_u32_e32 v140, 0xb000, v159
	ds_read2_b64 v[140:143], v140 offset0:232 offset1:234
	v_add_u32_e32 v144, 0xb000, v159
	ds_read2_b64 v[144:147], v144 offset0:236 offset1:238
	v_pk_mul_f32 v[66:67], v[66:67], v[200:201] op_sel_hi:[1,0]
	v_pk_mul_f32 v[64:65], v[64:65], v[200:201] op_sel_hi:[1,0]
	v_pk_mul_f32 v[62:63], v[62:63], v[200:201] op_sel_hi:[1,0]
	v_pk_mul_f32 v[60:61], v[60:61], v[200:201] op_sel_hi:[1,0]
	v_pk_mul_f32 v[58:59], v[58:59], v[200:201] op_sel_hi:[1,0]
	v_pk_mul_f32 v[56:57], v[56:57], v[200:201] op_sel_hi:[1,0]
	v_pk_mul_f32 v[54:55], v[54:55], v[200:201] op_sel_hi:[1,0]
	v_pk_mul_f32 v[52:53], v[52:53], v[200:201] op_sel_hi:[1,0]
	v_pk_mul_f32 v[50:51], v[50:51], v[200:201] op_sel_hi:[1,0]
	v_pk_mul_f32 v[48:49], v[48:49], v[200:201] op_sel_hi:[1,0]
	v_pk_mul_f32 v[46:47], v[46:47], v[200:201] op_sel_hi:[1,0]
	v_pk_mul_f32 v[44:45], v[44:45], v[200:201] op_sel_hi:[1,0]
	v_pk_mul_f32 v[42:43], v[42:43], v[200:201] op_sel_hi:[1,0]
	v_pk_mul_f32 v[40:41], v[40:41], v[200:201] op_sel_hi:[1,0]
	v_pk_mul_f32 v[38:39], v[38:39], v[200:201] op_sel_hi:[1,0]
	v_pk_mul_f32 v[36:37], v[36:37], v[200:201] op_sel_hi:[1,0]
	s_waitcnt lgkmcnt(0)
	v_mfma_f32_32x32x16_bf16 v[52:67], v[116:119], v[100:103], v[52:67]
	s_mov_b32 s26, 0x47200000
	v_add_co_u32_e32 v218, vcc, s26, v182
	s_nop 1
	v_addc_co_u32_e32 v219, vcc, 0, v183, vcc
	global_store_dword v[218:219], v68, off
	global_store_dword v[218:219], v69, off offset:2048
	v_mfma_f32_32x32x16_bf16 v[36:51], v[132:135], v[100:103], v[36:51]
	s_mov_b32 s26, 0x47201000
	v_add_co_u32_e32 v220, vcc, s26, v182
	s_nop 1
	v_addc_co_u32_e32 v221, vcc, 0, v183, vcc
	global_store_dword v[220:221], v70, off
	global_store_dword v[220:221], v71, off offset:2048
	v_mfma_f32_32x32x16_bf16 v[52:67], v[120:123], v[104:107], v[52:67]
	s_mov_b32 s26, 0x47204000
	v_add_co_u32_e32 v222, vcc, s26, v182
	s_nop 1
	v_addc_co_u32_e32 v223, vcc, 0, v183, vcc
	global_store_dword v[222:223], v72, off
	global_store_dword v[222:223], v73, off offset:2048
	v_mfma_f32_32x32x16_bf16 v[36:51], v[136:139], v[104:107], v[36:51]
	s_mov_b32 s26, 0x47205000
	v_add_co_u32_e32 v224, vcc, s26, v182
	s_nop 1
	v_addc_co_u32_e32 v225, vcc, 0, v183, vcc
	global_store_dword v[224:225], v74, off
	global_store_dword v[224:225], v75, off offset:2048
	v_mfma_f32_32x32x16_bf16 v[52:67], v[124:127], v[108:111], v[52:67]
	s_mov_b32 s26, 0x47208000
	v_add_co_u32_e32 v218, vcc, s26, v182
	s_nop 1
	v_addc_co_u32_e32 v219, vcc, 0, v183, vcc
	global_store_dword v[218:219], v76, off
	global_store_dword v[218:219], v77, off offset:2048
	v_mfma_f32_32x32x16_bf16 v[36:51], v[140:143], v[108:111], v[36:51]
	s_mov_b32 s26, 0x47209000
	v_add_co_u32_e32 v220, vcc, s26, v182
	s_nop 1
	v_addc_co_u32_e32 v221, vcc, 0, v183, vcc
	global_store_dword v[220:221], v78, off
	global_store_dword v[220:221], v79, off offset:2048
	v_mfma_f32_32x32x16_bf16 v[52:67], v[128:131], v[112:115], v[52:67]
	s_mov_b32 s26, 0x4720c000
	v_add_co_u32_e32 v222, vcc, s26, v182
	s_nop 1
	v_addc_co_u32_e32 v223, vcc, 0, v183, vcc
	global_store_dword v[222:223], v80, off
	global_store_dword v[222:223], v81, off offset:2048
	v_mfma_f32_32x32x16_bf16 v[36:51], v[144:147], v[112:115], v[36:51]
	s_mov_b32 s26, 0x4720d000
	v_add_co_u32_e32 v224, vcc, s26, v182
	s_nop 1
	v_addc_co_u32_e32 v225, vcc, 0, v183, vcc
	global_store_dword v[224:225], v82, off
	global_store_dword v[224:225], v83, off offset:2048
	v_add_u32_e32 v116, 0xc800, v159
	ds_read2_b64 v[116:119], v116 offset1:2
	v_add_u32_e32 v120, 0xc800, v159
	ds_read2_b64 v[120:123], v120 offset0:4 offset1:6
	v_add_u32_e32 v124, 0xc800, v159
	ds_read2_b64 v[124:127], v124 offset0:8 offset1:10
	v_add_u32_e32 v128, 0xc800, v159
	ds_read2_b64 v[128:131], v128 offset0:12 offset1:14
	v_add_u32_e32 v132, 0xd800, v159
	ds_read2_b64 v[132:135], v132 offset0:32 offset1:34
	v_add_u32_e32 v136, 0xd800, v159
	ds_read2_b64 v[136:139], v136 offset0:36 offset1:38
	v_add_u32_e32 v140, 0xd800, v159
	ds_read2_b64 v[140:143], v140 offset0:40 offset1:42
	v_add_u32_e32 v144, 0xd800, v159
	ds_read2_b64 v[144:147], v144 offset0:44 offset1:46
	v_pk_mul_f32 v[34:35], v[34:35], v[200:201] op_sel_hi:[1,0]
	v_pk_mul_f32 v[32:33], v[32:33], v[200:201] op_sel_hi:[1,0]
	v_pk_mul_f32 v[30:31], v[30:31], v[200:201] op_sel_hi:[1,0]
	v_pk_mul_f32 v[28:29], v[28:29], v[200:201] op_sel_hi:[1,0]
	v_pk_mul_f32 v[26:27], v[26:27], v[200:201] op_sel_hi:[1,0]
	v_pk_mul_f32 v[24:25], v[24:25], v[200:201] op_sel_hi:[1,0]
	v_pk_mul_f32 v[22:23], v[22:23], v[200:201] op_sel_hi:[1,0]
	v_pk_mul_f32 v[20:21], v[20:21], v[200:201] op_sel_hi:[1,0]
	v_pk_mul_f32 v[18:19], v[18:19], v[200:201] op_sel_hi:[1,0]
	v_pk_mul_f32 v[16:17], v[16:17], v[200:201] op_sel_hi:[1,0]
	v_pk_mul_f32 v[14:15], v[14:15], v[200:201] op_sel_hi:[1,0]
	v_pk_mul_f32 v[12:13], v[12:13], v[200:201] op_sel_hi:[1,0]
	v_pk_mul_f32 v[10:11], v[10:11], v[200:201] op_sel_hi:[1,0]
	v_pk_mul_f32 v[8:9], v[8:9], v[200:201] op_sel_hi:[1,0]
	v_pk_mul_f32 v[6:7], v[6:7], v[200:201] op_sel_hi:[1,0]
	v_pk_mul_f32 v[4:5], v[4:5], v[200:201] op_sel_hi:[1,0]
	s_waitcnt lgkmcnt(0)
	v_mfma_f32_32x32x16_bf16 v[20:35], v[116:119], v[100:103], v[20:35]
	s_mov_b32 s26, 0x47210000
	v_add_co_u32_e32 v218, vcc, s26, v182
	s_nop 1
	v_addc_co_u32_e32 v219, vcc, 0, v183, vcc
	global_store_dword v[218:219], v84, off
	global_store_dword v[218:219], v85, off offset:2048
	v_mfma_f32_32x32x16_bf16 v[4:19], v[132:135], v[100:103], v[4:19]
	s_mov_b32 s26, 0x47211000
	v_add_co_u32_e32 v220, vcc, s26, v182
	s_nop 1
	v_addc_co_u32_e32 v221, vcc, 0, v183, vcc
	global_store_dword v[220:221], v86, off
	global_store_dword v[220:221], v87, off offset:2048
	v_mfma_f32_32x32x16_bf16 v[20:35], v[120:123], v[104:107], v[20:35]
	s_mov_b32 s26, 0x47214000
	v_add_co_u32_e32 v222, vcc, s26, v182
	s_nop 1
	v_addc_co_u32_e32 v223, vcc, 0, v183, vcc
	global_store_dword v[222:223], v88, off
	global_store_dword v[222:223], v89, off offset:2048
	v_mfma_f32_32x32x16_bf16 v[4:19], v[136:139], v[104:107], v[4:19]
	s_mov_b32 s26, 0x47215000
	v_add_co_u32_e32 v224, vcc, s26, v182
	s_nop 1
	v_addc_co_u32_e32 v225, vcc, 0, v183, vcc
	global_store_dword v[224:225], v90, off
	global_store_dword v[224:225], v91, off offset:2048
	v_mfma_f32_32x32x16_bf16 v[20:35], v[124:127], v[108:111], v[20:35]
	s_mov_b32 s26, 0x47218000
	v_add_co_u32_e32 v218, vcc, s26, v182
	s_nop 1
	v_addc_co_u32_e32 v219, vcc, 0, v183, vcc
	global_store_dword v[218:219], v92, off
	global_store_dword v[218:219], v93, off offset:2048
	v_mfma_f32_32x32x16_bf16 v[4:19], v[140:143], v[108:111], v[4:19]
	s_mov_b32 s26, 0x47219000
	v_add_co_u32_e32 v220, vcc, s26, v182
	s_nop 1
	v_addc_co_u32_e32 v221, vcc, 0, v183, vcc
	global_store_dword v[220:221], v94, off
	global_store_dword v[220:221], v95, off offset:2048
	v_mfma_f32_32x32x16_bf16 v[20:35], v[128:131], v[112:115], v[20:35]
	s_mov_b32 s26, 0x4721c000
	v_add_co_u32_e32 v222, vcc, s26, v182
	s_nop 1
	v_addc_co_u32_e32 v223, vcc, 0, v183, vcc
	global_store_dword v[222:223], v96, off
	global_store_dword v[222:223], v97, off offset:2048
	v_mfma_f32_32x32x16_bf16 v[4:19], v[144:147], v[112:115], v[4:19]
	s_mov_b32 s26, 0x4721d000
	v_add_co_u32_e32 v224, vcc, s26, v182
	s_nop 1
	v_addc_co_u32_e32 v225, vcc, 0, v183, vcc
	global_store_dword v[224:225], v98, off
	global_store_dword v[224:225], v99, off offset:2048
	v_lshrrev_b32_e32 v226, 5, v230
	v_lshlrev_b32_e32 v226, 2, v226
	v_sub_u32_e32 v226, v230, v226
	v_lshlrev_b32_e32 v226, 11, v226
	v_and_b32_e32 v227, 31, v230
	v_lshlrev_b32_e32 v227, 2, v227
	v_sub_u32_e32 v226, v226, v227
	v_add_u32_e32 v226, 0x41a40000, v226
	v_add_co_u32_e32 v226, vcc, v226, v182
	s_nop 1
	v_addc_co_u32_e32 v227, vcc, 0, v183, vcc
	global_load_dword v240, v[226:227], off
	s_add_u32 s28, s28, 4
	s_addc_u32 s29, s29, 0
	v_lshl_add_u64 v[162:163], v[162:163], 0, s[38:39]
	s_cmp_eq_u32 s35, 63
	s_barrier
	s_cbranch_scc0 .LBB0_490
	s_waitcnt vmcnt(0)
	v_mov_b32_e32 v226, 0x44ffe000
	v_mov_b32_e32 v227, 0x3b808081
	v_mov_b32_e32 v240, 0x43e00000
	v_add_u32_e32 v82, v157, v155
	v_cvt_pk_bf16_f32 v52, v52, v53
	v_cvt_pk_bf16_f32 v53, v54, v55
	v_cvt_pk_bf16_f32 v54, v56, v57
	v_cvt_pk_bf16_f32 v57, v62, v63
	v_cvt_pk_bf16_f32 v62, v8, v9
	v_add_u32_e32 v8, 0xe800, v82
	v_cvt_pk_bf16_f32 v56, v60, v61
	v_cvt_pk_bf16_f32 v36, v36, v37
	v_cvt_pk_bf16_f32 v37, v38, v39
	v_cvt_pk_bf16_f32 v38, v40, v41
	v_cvt_pk_bf16_f32 v39, v42, v43
	v_cvt_pk_bf16_f32 v40, v44, v45
	v_cvt_pk_bf16_f32 v41, v46, v47
	v_cvt_pk_bf16_f32 v42, v48, v49
	v_cvt_pk_bf16_f32 v43, v50, v51
	v_cvt_pk_bf16_f32 v44, v20, v21
	v_cvt_pk_bf16_f32 v45, v22, v23
	v_cvt_pk_bf16_f32 v46, v24, v25
	v_cvt_pk_bf16_f32 v47, v26, v27
	v_cvt_pk_bf16_f32 v48, v28, v29
	v_cvt_pk_bf16_f32 v49, v30, v31
	v_cvt_pk_bf16_f32 v50, v32, v33
	v_cvt_pk_bf16_f32 v51, v34, v35
	v_cvt_pk_bf16_f32 v60, v4, v5
	v_cvt_pk_bf16_f32 v61, v6, v7
	ds_read2_b64 v[4:7], v8 offset0:64 offset1:66
	ds_read2_b64 v[20:23], v8 offset0:68 offset1:70
	ds_read2_b64 v[24:27], v8 offset0:72 offset1:74
	ds_read2_b64 v[28:31], v8 offset0:76 offset1:78
	ds_read2_b64 v[32:35], v8 offset0:80 offset1:82
	ds_read2_b64 v[68:71], v8 offset0:84 offset1:86
	ds_read2_b64 v[72:75], v8 offset0:88 offset1:90
	ds_read2_b64 v[78:81], v8 offset0:92 offset1:94
	s_add_u32 s24, s6, s24
	s_addc_u32 s25, s7, s25
	s_add_u32 s24, s24, s9
	s_addc_u32 s25, s25, 0
	v_lshl_add_u64 v[76:77], v[160:161], 2, s[24:25]
	v_cvt_pk_bf16_f32 v55, v58, v59
	v_cvt_pk_bf16_f32 v58, v64, v65
	v_cvt_pk_bf16_f32 v59, v66, v67
	v_cvt_pk_bf16_f32 v63, v10, v11
	v_cvt_pk_bf16_f32 v64, v12, v13
	v_cvt_pk_bf16_f32 v65, v14, v15
	v_cvt_pk_bf16_f32 v66, v16, v17
	v_cvt_pk_bf16_f32 v67, v18, v19
	s_waitcnt lgkmcnt(7)
	v_mfma_f32_32x32x16_bf16 v[4:19], v[4:7], v[52:55], 0
	s_waitcnt lgkmcnt(6)
	v_mfma_f32_32x32x16_bf16 v[4:19], v[20:23], v[56:59], v[4:19]
	s_waitcnt lgkmcnt(5)
	v_mfma_f32_32x32x16_bf16 v[4:19], v[24:27], v[36:39], v[4:19]
	s_waitcnt lgkmcnt(4)
	v_mfma_f32_32x32x16_bf16 v[4:19], v[28:31], v[40:43], v[4:19]
	s_waitcnt lgkmcnt(3)
	v_mfma_f32_32x32x16_bf16 v[4:19], v[32:35], v[44:47], v[4:19]
	s_waitcnt lgkmcnt(2)
	v_mfma_f32_32x32x16_bf16 v[4:19], v[68:71], v[48:51], v[4:19]
	s_waitcnt lgkmcnt(1)
	v_mfma_f32_32x32x16_bf16 v[4:19], v[72:75], v[60:63], v[4:19]
	s_waitcnt lgkmcnt(0)
	v_mfma_f32_32x32x16_bf16 v[4:19], v[78:81], v[64:67], v[4:19]
	v_add_u32_e32 v20, 0x2100, v82
	v_add_u32_e32 v24, 0xe800, v20
	ds_read2_b64 v[20:23], v24 offset0:64 offset1:66
	ds_read2_b64 v[68:71], v24 offset0:68 offset1:70
	ds_read2_b64 v[72:75], v24 offset0:72 offset1:74
	ds_read2_b64 v[78:81], v24 offset0:76 offset1:78
	ds_read2_b64 v[82:85], v24 offset0:80 offset1:82
	ds_read2_b64 v[86:89], v24 offset0:84 offset1:86
	ds_read2_b64 v[90:93], v24 offset0:88 offset1:90
	ds_read2_b64 v[94:97], v24 offset0:92 offset1:94
	s_waitcnt lgkmcnt(7)
	v_mfma_f32_32x32x16_bf16 v[20:35], v[20:23], v[52:55], 0
	s_waitcnt lgkmcnt(6)
	v_mfma_f32_32x32x16_bf16 v[20:35], v[68:71], v[56:59], v[20:35]
	s_waitcnt lgkmcnt(5)
	v_mfma_f32_32x32x16_bf16 v[20:35], v[72:75], v[36:39], v[20:35]
	s_waitcnt lgkmcnt(4)
	v_mfma_f32_32x32x16_bf16 v[20:35], v[78:81], v[40:43], v[20:35]
	s_waitcnt lgkmcnt(3)
	v_mfma_f32_32x32x16_bf16 v[20:35], v[82:85], v[44:47], v[20:35]
	s_waitcnt lgkmcnt(2)
	v_mfma_f32_32x32x16_bf16 v[20:35], v[86:89], v[48:51], v[20:35]
	s_waitcnt lgkmcnt(1)
	v_mfma_f32_32x32x16_bf16 v[20:35], v[90:93], v[60:63], v[20:35]
	s_waitcnt lgkmcnt(0)
	v_mfma_f32_32x32x16_bf16 v[20:35], v[94:97], v[64:67], v[20:35]
	v_add_f32_e64 v4, v166, -v4
	v_add_f32_e64 v5, v167, -v5
	v_add_f32_e64 v6, v164, -v6
	v_add_f32_e64 v7, v165, -v7
	v_add_f32_e64 v8, v168, -v8
	v_add_f32_e64 v9, v169, -v9
	v_pk_add_f32 v[10:11], v[170:171], v[10:11] neg_lo:[0,1] neg_hi:[0,1]
	v_pk_add_f32 v[12:13], v[180:181], v[12:13] neg_lo:[0,1] neg_hi:[0,1]
	v_pk_add_f32 v[14:15], v[194:195], v[14:15] neg_lo:[0,1] neg_hi:[0,1]
	v_pk_add_f32 v[16:17], v[196:197], v[16:17] neg_lo:[0,1] neg_hi:[0,1]
	v_pk_add_f32 v[18:19], v[198:199], v[18:19] neg_lo:[0,1] neg_hi:[0,1]
	v_cvt_pk_bf16_f32 v68, v4, v5
	v_cvt_pk_bf16_f32 v69, v6, v7
	v_pk_add_f32 v[4:5], v[172:173], v[20:21] neg_lo:[0,1] neg_hi:[0,1]
	v_pk_add_f32 v[6:7], v[174:175], v[22:23] neg_lo:[0,1] neg_hi:[0,1]
	v_add3_u32 v98, s31, v149, v155
	v_cvt_pk_bf16_f32 v70, v8, v9
	v_cvt_pk_bf16_f32 v71, v10, v11
	v_cvt_pk_bf16_f32 v72, v12, v13
	v_cvt_pk_bf16_f32 v73, v14, v15
	v_cvt_pk_bf16_f32 v74, v16, v17
	v_cvt_pk_bf16_f32 v75, v18, v19
	v_pk_add_f32 v[8:9], v[176:177], v[24:25] neg_lo:[0,1] neg_hi:[0,1]
	v_pk_add_f32 v[10:11], v[178:179], v[26:27] neg_lo:[0,1] neg_hi:[0,1]
	v_pk_add_f32 v[12:13], v[202:203], v[28:29] neg_lo:[0,1] neg_hi:[0,1]
	v_pk_add_f32 v[14:15], v[204:205], v[30:31] neg_lo:[0,1] neg_hi:[0,1]
	v_pk_add_f32 v[16:17], v[206:207], v[32:33] neg_lo:[0,1] neg_hi:[0,1]
	v_pk_add_f32 v[18:19], v[208:209], v[34:35] neg_lo:[0,1] neg_hi:[0,1]
	v_cvt_pk_bf16_f32 v78, v4, v5
	v_cvt_pk_bf16_f32 v79, v6, v7
	ds_read2_b64 v[4:7], v98 offset1:2
	ds_read2_b64 v[20:23], v98 offset0:4 offset1:6
	ds_read2_b64 v[24:27], v98 offset0:8 offset1:10
	ds_read2_b64 v[28:31], v98 offset0:12 offset1:14
	ds_read2_b64 v[32:35], v98 offset0:16 offset1:18
	ds_read2_b64 v[82:85], v98 offset0:20 offset1:22
	ds_read2_b64 v[86:89], v98 offset0:24 offset1:26
	ds_read2_b64 v[90:93], v98 offset0:28 offset1:30
	v_cvt_pk_bf16_f32 v80, v8, v9
	v_cvt_pk_bf16_f32 v81, v10, v11
	v_cvt_pk_bf16_f32 v94, v12, v13
	v_cvt_pk_bf16_f32 v95, v14, v15
	v_cvt_pk_bf16_f32 v96, v16, v17
	v_cvt_pk_bf16_f32 v97, v18, v19
	s_waitcnt lgkmcnt(7)
	v_mfma_f32_32x32x16_bf16 v[4:19], v[4:7], v[52:55], 0
	s_waitcnt lgkmcnt(6)
	v_mfma_f32_32x32x16_bf16 v[4:19], v[20:23], v[56:59], v[4:19]
	s_waitcnt lgkmcnt(5)
	v_mfma_f32_32x32x16_bf16 v[4:19], v[24:27], v[36:39], v[4:19]
	s_waitcnt lgkmcnt(4)
	v_mfma_f32_32x32x16_bf16 v[4:19], v[28:31], v[40:43], v[4:19]
	s_waitcnt lgkmcnt(3)
	v_mfma_f32_32x32x16_bf16 v[4:19], v[32:35], v[44:47], v[4:19]
	s_waitcnt lgkmcnt(2)
	v_mfma_f32_32x32x16_bf16 v[4:19], v[82:85], v[48:51], v[4:19]
	s_waitcnt lgkmcnt(1)
	v_mfma_f32_32x32x16_bf16 v[4:19], v[86:89], v[60:63], v[4:19]
	s_waitcnt lgkmcnt(0)
	v_mfma_f32_32x32x16_bf16 v[4:19], v[90:93], v[64:67], v[4:19]
	v_add_u32_e32 v24, 0x2000, v98
	ds_read2_b64 v[20:23], v24 offset0:32 offset1:34
	ds_read2_b64 v[82:85], v24 offset0:36 offset1:38
	ds_read2_b64 v[86:89], v24 offset0:40 offset1:42
	ds_read2_b64 v[90:93], v24 offset0:44 offset1:46
	ds_read2_b64 v[98:101], v24 offset0:48 offset1:50
	ds_read2_b64 v[102:105], v24 offset0:52 offset1:54
	ds_read2_b64 v[106:109], v24 offset0:56 offset1:58
	ds_read2_b64 v[110:113], v24 offset0:60 offset1:62
	s_waitcnt lgkmcnt(7)
	v_mfma_f32_32x32x16_bf16 v[20:35], v[20:23], v[52:55], 0
	s_waitcnt lgkmcnt(6)
	v_mfma_f32_32x32x16_bf16 v[20:35], v[82:85], v[56:59], v[20:35]
	s_waitcnt lgkmcnt(5)
	v_mfma_f32_32x32x16_bf16 v[20:35], v[86:89], v[36:39], v[20:35]
	s_waitcnt lgkmcnt(4)
	v_mfma_f32_32x32x16_bf16 v[20:35], v[90:93], v[40:43], v[20:35]
	s_waitcnt lgkmcnt(3)
	v_mfma_f32_32x32x16_bf16 v[20:35], v[98:101], v[44:47], v[20:35]
	s_waitcnt lgkmcnt(2)
	v_mfma_f32_32x32x16_bf16 v[20:35], v[102:105], v[48:51], v[20:35]
	s_waitcnt lgkmcnt(1)
	v_mfma_f32_32x32x16_bf16 v[20:35], v[106:109], v[60:63], v[20:35]
	s_waitcnt lgkmcnt(0)
	v_mfma_f32_32x32x16_bf16 v[20:35], v[110:113], v[64:67], v[20:35]
	v_add3_u32 v52, s33, v149, v153
	v_add_u32_e32 v64, 0x1000, v52
	ds_read2_b64 v[36:39], v52 offset1:2
	ds_read2_b64 v[40:43], v52 offset0:4 offset1:6
	ds_read2_b64 v[44:47], v52 offset0:8 offset1:10
	ds_read2_b64 v[48:51], v52 offset0:12 offset1:14
	ds_read2_b64 v[52:55], v64 offset0:32 offset1:34
	ds_read2_b64 v[56:59], v64 offset0:36 offset1:38
	ds_read2_b64 v[60:63], v64 offset0:40 offset1:42
	ds_read2_b64 v[64:67], v64 offset0:44 offset1:46
	s_waitcnt lgkmcnt(7)
	v_mfma_f32_32x32x16_bf16 v[4:19], v[36:39], v[68:71], v[4:19]
	s_waitcnt lgkmcnt(3)
	v_mfma_f32_32x32x16_bf16 v[20:35], v[52:55], v[68:71], v[20:35]
	v_mfma_f32_32x32x16_bf16 v[4:19], v[40:43], v[72:75], v[4:19]
	s_waitcnt lgkmcnt(2)
	v_mfma_f32_32x32x16_bf16 v[20:35], v[56:59], v[72:75], v[20:35]
	v_mfma_f32_32x32x16_bf16 v[4:19], v[44:47], v[78:81], v[4:19]
	s_waitcnt lgkmcnt(1)
	v_mfma_f32_32x32x16_bf16 v[20:35], v[60:63], v[78:81], v[20:35]
	v_mfma_f32_32x32x16_bf16 v[4:19], v[48:51], v[94:97], v[4:19]
	s_waitcnt lgkmcnt(0)
	v_mfma_f32_32x32x16_bf16 v[20:35], v[64:67], v[94:97], v[20:35]
	v_lshl_add_u64 v[36:37], v[76:77], 0, v[2:3]
	s_mov_b32 s9, 0x479e0000
	v_add_co_u32_e32 v38, vcc, s9, v36
	s_mov_b32 s9, 0x479e1000
	s_nop 0
	v_addc_co_u32_e32 v39, vcc, 0, v37, vcc
	s_nop 3
	global_store_dword v[38:39], v4, off
	global_store_dword v[38:39], v5, off offset:2048
	v_add_co_u32_e32 v4, vcc, s9, v36
	s_mov_b32 s9, 0x479e4000
	s_nop 0
	v_addc_co_u32_e32 v5, vcc, 0, v37, vcc
	global_store_dword v[4:5], v6, off
	global_store_dword v[4:5], v7, off offset:2048
	v_add_co_u32_e32 v4, vcc, s9, v36
	s_mov_b32 s9, 0x479e5000
	s_nop 0
	v_addc_co_u32_e32 v5, vcc, 0, v37, vcc
	global_store_dword v[4:5], v8, off
	global_store_dword v[4:5], v9, off offset:2048
	v_add_co_u32_e32 v4, vcc, s9, v36
	s_mov_b32 s9, 0x479e8000
	s_nop 0
	v_addc_co_u32_e32 v5, vcc, 0, v37, vcc
	global_store_dword v[4:5], v10, off
	global_store_dword v[4:5], v11, off offset:2048
	v_add_co_u32_e32 v4, vcc, s9, v36
	s_mov_b32 s9, 0x479e9000
	s_nop 0
	v_addc_co_u32_e32 v5, vcc, 0, v37, vcc
	global_store_dword v[4:5], v12, off
	global_store_dword v[4:5], v13, off offset:2048
	v_add_co_u32_e32 v4, vcc, s9, v36
	s_mov_b32 s9, 0x479ec000
	s_nop 0
	v_addc_co_u32_e32 v5, vcc, 0, v37, vcc
	global_store_dword v[4:5], v14, off
	global_store_dword v[4:5], v15, off offset:2048
	v_add_co_u32_e32 v4, vcc, s9, v36
	s_mov_b32 s9, 0x479ed000
	s_nop 0
	v_addc_co_u32_e32 v5, vcc, 0, v37, vcc
	global_store_dword v[4:5], v16, off
	global_store_dword v[4:5], v17, off offset:2048
	v_add_co_u32_e32 v4, vcc, s9, v36
	s_mov_b32 s9, 0x479f0000
	s_nop 0
	v_addc_co_u32_e32 v5, vcc, 0, v37, vcc
	global_store_dword v[4:5], v18, off
	global_store_dword v[4:5], v19, off offset:2048
	v_add_co_u32_e32 v4, vcc, s9, v36
	s_mov_b32 s9, 0x479f1000
	s_nop 0
	v_addc_co_u32_e32 v5, vcc, 0, v37, vcc
	global_store_dword v[4:5], v20, off
	global_store_dword v[4:5], v21, off offset:2048
	v_add_co_u32_e32 v4, vcc, s9, v36
	s_mov_b32 s9, 0x479f4000
	s_nop 0
	v_addc_co_u32_e32 v5, vcc, 0, v37, vcc
	global_store_dword v[4:5], v22, off
	global_store_dword v[4:5], v23, off offset:2048
	v_add_co_u32_e32 v4, vcc, s9, v36
	s_mov_b32 s9, 0x479f5000
	s_nop 0
	v_addc_co_u32_e32 v5, vcc, 0, v37, vcc
	global_store_dword v[4:5], v24, off
	global_store_dword v[4:5], v25, off offset:2048
	v_add_co_u32_e32 v4, vcc, s9, v36
	s_mov_b32 s9, 0x479f8000
	s_nop 0
	v_addc_co_u32_e32 v5, vcc, 0, v37, vcc
	global_store_dword v[4:5], v26, off
	global_store_dword v[4:5], v27, off offset:2048
	v_add_co_u32_e32 v4, vcc, s9, v36
	s_mov_b32 s9, 0x479f9000
	s_nop 0
	v_addc_co_u32_e32 v5, vcc, 0, v37, vcc
	global_store_dword v[4:5], v28, off
	global_store_dword v[4:5], v29, off offset:2048
	v_add_co_u32_e32 v4, vcc, s9, v36
	s_mov_b32 s9, 0x479fc000
	s_nop 0
	v_addc_co_u32_e32 v5, vcc, 0, v37, vcc
	global_store_dword v[4:5], v30, off
	global_store_dword v[4:5], v31, off offset:2048
	v_add_co_u32_e32 v4, vcc, s9, v36
	s_nop 1
	v_addc_co_u32_e32 v5, vcc, 0, v37, vcc
	global_store_dword v[4:5], v32, off
	global_store_dword v[4:5], v33, off offset:2048
	v_add_co_u32_e32 v4, vcc, 0x479fd000, v36
	s_nop 1
	v_addc_co_u32_e32 v5, vcc, 0, v37, vcc
	global_store_dword v[4:5], v34, off
	global_store_dword v[4:5], v35, off offset:2048
	s_mov_b64 s[28:29], 0
	s_waitcnt lgkmcnt(0)
	s_barrier
